# speedup vs baseline: 1.0013x; 1.0013x over previous
_Z11attn_kernelPKDF16_S0_PDF16_P15HIP_vector_typeIfLj2EE:
	s_lshl_b32 s40, s3, 4
	s_add_u32 s40, s40, s2
	s_lshl_b32 s41, s4, 6
	s_add_u32 s40, s40, s41
	s_and_b32 s41, s40, 7
	s_lshr_b32 s40, s40, 3
	s_and_b32 s2, s41, 3
	s_lshl_b32 s2, s2, 2
	s_and_b32 s3, s40, 3
	s_or_b32 s2, s2, s3
	s_lshr_b32 s3, s40, 2
	s_and_b32 s3, s3, 3
	s_lshr_b32 s4, s41, 2
	s_lshl_b32 s4, s4, 1
	s_lshr_b32 s40, s40, 4
	s_or_b32 s4, s4, s40
	s_mov_b32 s5, 0
	s_mov_b32 s28, s3
	s_load_dwordx8 s[20:27], s[0:1], 0x0
	s_mov_b32 s3, s5
	s_lshl_b64 s[0:1], s[4:5], 12
	s_lshl_b64 s[2:3], s[2:3], 8
	s_add_u32 s0, s0, s2
	v_lshrrev_b32_e32 v1, 6, v0
	s_addc_u32 s1, s1, s3
	v_and_b32_e32 v160, 31, v0
	s_lshl_b64 s[2:3], s[0:1], 8
	v_lshlrev_b32_e32 v162, 5, v1
	s_waitcnt lgkmcnt(0)
	s_add_u32 s2, s20, s2
	v_or_b32_e32 v2, v162, v160
	v_bfe_u32 v54, v0, 5, 1
	s_addc_u32 s3, s21, s3
	v_and_b32_e32 v164, 63, v0
	v_lshrrev_b32_e32 v165, 4, v164
	v_add_u32_e32 v165, v162, v165
	v_lshlrev_b32_e32 v165, 8, v165
	v_and_b32_e32 v164, 15, v164
	v_lshl_add_u32 v164, v164, 4, v165
	v_mov_b32_e32 v165, 0
	v_lshl_add_u64 v[2:3], s[2:3], 0, v[164:165]
	s_mov_b64 s[6:7], 0x1000
	v_lshl_add_u64 v[4:5], v[2:3], 0, s[6:7]
	global_load_dwordx4 v[156:159], v[2:3], off
	global_load_dwordx4 v[152:155], v[2:3], off offset:1024
	global_load_dwordx4 v[148:151], v[2:3], off offset:2048
	global_load_dwordx4 v[144:147], v[2:3], off offset:3072
	global_load_dwordx4 v[140:143], v[4:5], off
	global_load_dwordx4 v[136:139], v[4:5], off offset:1024
	global_load_dwordx4 v[132:135], v[4:5], off offset:2048
	global_load_dwordx4 v[128:131], v[4:5], off offset:3072
	v_lshlrev_b32_e32 v164, 4, v54
	s_ashr_i32 s29, s28, 31
	v_bfe_u32 v55, v0, 2, 3
	s_lshl_b64 s[2:3], s[4:5], 20
	s_lshl_b64 s[20:21], s[28:29], 18
	v_lshl_or_b32 v2, v1, 3, v55
	s_add_u32 s4, s22, s2
	v_lshrrev_b32_e32 v3, 2, v2
	s_addc_u32 s7, s23, s3
	v_xor_b32_e32 v4, v3, v0
	s_add_u32 s6, s4, s20
	v_and_b32_e32 v5, 32, v0
	v_lshlrev_b32_e32 v4, 3, v4
	v_lshlrev_b32_e32 v1, 11, v1
	s_addc_u32 s7, s7, s21
	v_lshlrev_b32_e32 v164, 8, v2
	v_and_or_b32 v4, v4, 24, v5
	v_add_u32_e32 v173, 0, v1
	v_lshl_add_u64 v[2:3], s[6:7], 0, v[164:165]
	v_lshlrev_b32_e32 v164, 1, v4
	v_readfirstlane_b32 s4, v173
	v_add_u32_e32 v6, 0x400, v173
	v_lshl_add_u64 v[2:3], v[2:3], 0, v[164:165]
	s_mov_b64 s[6:7], 0x80
	s_mov_b32 m0, s4
	v_readfirstlane_b32 s4, v6
	v_add_u32_e32 v6, 0x4000, v173
	v_lshl_add_u64 v[4:5], v[2:3], 0, s[6:7]
	global_load_lds_dwordx4 v[2:3], off
	s_mov_b32 m0, s4
	s_mov_b64 s[6:7], 0x4000
	v_readfirstlane_b32 s4, v6
	global_load_lds_dwordx4 v[4:5], off
	v_lshl_add_u64 v[4:5], v[2:3], 0, s[6:7]
	s_mov_b32 m0, s4
	s_mov_b64 s[6:7], 0x4080
	global_load_lds_dwordx4 v[4:5], off
	v_add_u32_e32 v4, 0x4400, v173
	v_lshl_add_u64 v[2:3], v[2:3], 0, s[6:7]
	v_readfirstlane_b32 s4, v4
	s_mov_b32 m0, s4
	s_movk_i32 s4, 0x1c0
	global_load_lds_dwordx4 v[2:3], off
	v_lshlrev_b32_e32 v2, 8, v0
	v_and_b32_e32 v2, 0x1800, v2
	v_lshlrev_b32_e32 v3, 6, v0
	v_and_or_b32 v6, v3, s4, v2
	v_xor_b32_e32 v2, v54, v55
	v_lshlrev_b32_e32 v2, 4, v2
	v_and_or_b32 v175, v2, 48, v6
	v_and_b32_e32 v190, 63, v0
	v_lshrrev_b32_e32 v191, 4, v190
	v_and_b32_e32 v192, 15, v190
	v_xor_b32_e32 v193, v192, v191
	v_lshlrev_b32_e32 v193, 4, v193
	v_add_u32_e32 v194, v162, v191
	v_lshlrev_b32_e32 v194, 8, v194
	v_add_u32_e32 v194, 0x10000, v194
	v_and_b32_e32 v195, 15, v160
	v_xor_b32_e32 v195, v195, v54
	v_lshlrev_b32_e32 v195, 4, v195
	v_add_u32_e32 v196, v162, v160
	v_lshlrev_b32_e32 v196, 8, v196
	v_add_u32_e32 v196, 0x10000, v196
	s_waitcnt vmcnt(4)
	v_xor_b32_e32 v197, 0x0, v193
	v_add_u32_e32 v197, v197, v194
	ds_write_b128 v197, v[156:159] offset:0
	v_xor_b32_e32 v197, 0x40, v193
	v_add_u32_e32 v197, v197, v194
	ds_write_b128 v197, v[152:155] offset:1024
	v_xor_b32_e32 v197, 0x80, v193
	v_add_u32_e32 v197, v197, v194
	ds_write_b128 v197, v[148:151] offset:2048
	v_xor_b32_e32 v197, 0xc0, v193
	v_add_u32_e32 v197, v197, v194
	ds_write_b128 v197, v[144:147] offset:3072
	v_xor_b32_e32 v197, 0x0, v193
	v_add_u32_e32 v197, v197, v194
	ds_write_b128 v197, v[140:143] offset:4096
	v_xor_b32_e32 v197, 0x40, v193
	v_add_u32_e32 v197, v197, v194
	ds_write_b128 v197, v[136:139] offset:5120
	v_xor_b32_e32 v197, 0x80, v193
	v_add_u32_e32 v197, v197, v194
	ds_write_b128 v197, v[132:135] offset:6144
	v_xor_b32_e32 v197, 0xc0, v193
	v_add_u32_e32 v197, v197, v194
	ds_write_b128 v197, v[128:131] offset:7168
	s_waitcnt lgkmcnt(0)
	v_xor_b32_e32 v198, 0x0, v195
	v_add_u32_e32 v198, v198, v196
	ds_read_b128 v[156:159], v198
	v_xor_b32_e32 v198, 0x20, v195
	v_add_u32_e32 v198, v198, v196
	ds_read_b128 v[152:155], v198
	v_xor_b32_e32 v198, 0x40, v195
	v_add_u32_e32 v198, v198, v196
	ds_read_b128 v[148:151], v198
	v_xor_b32_e32 v198, 0x60, v195
	v_add_u32_e32 v198, v198, v196
	ds_read_b128 v[144:147], v198
	v_xor_b32_e32 v198, 0x80, v195
	v_add_u32_e32 v198, v198, v196
	ds_read_b128 v[140:143], v198
	v_xor_b32_e32 v198, 0xa0, v195
	v_add_u32_e32 v198, v198, v196
	ds_read_b128 v[136:139], v198
	v_xor_b32_e32 v198, 0xc0, v195
	v_add_u32_e32 v198, v198, v196
	ds_read_b128 v[132:135], v198
	v_xor_b32_e32 v198, 0xe0, v195
	v_add_u32_e32 v198, v198, v196
	ds_read_b128 v[128:131], v198
	s_waitcnt vmcnt(2)
	v_add_u32_e32 v172, 0, v175
	s_waitcnt lgkmcnt(0)
	s_barrier
	ds_read_b128 v[2:5], v172
	ds_read_b128 v[34:37], v172 offset:512
	v_bitop3_b32 v7, v54, v55, 2 bitop3:0x36
	v_lshlrev_b32_e32 v7, 4, v7
	v_and_or_b32 v176, v7, 48, v6
	v_add_u32_e32 v174, 0, v176
	ds_read_b128 v[18:21], v174
	ds_read_b128 v[38:41], v174 offset:512
	s_mov_b32 s33, 0x41200000
	s_cmp_lg_u32 0, -1
	s_cselect_b32 s37, 0, 0
	s_waitcnt vmcnt(2) lgkmcnt(0)
	v_mfma_f32_32x32x16_f16 v[2:17], v[2:5], v[156:159], 0
	s_movk_i32 s4, 0x110
	v_and_b32_e32 v161, 63, v0
	v_lshl_or_b32 v1, v55, 8, v1
	s_mov_b32 s18, s5
	s_mov_b32 s19, s5
	s_mov_b32 s6, s5
	s_mov_b32 s7, s5
	v_mfma_f32_32x32x16_f16 v[2:17], v[18:21], v[152:155], v[2:17]
	ds_read_b128 v[18:21], v172 offset:8192
	ds_read_b128 v[42:45], v172 offset:8704
	ds_read_b128 v[46:49], v174 offset:8192
	ds_read_b128 v[50:53], v174 offset:8704
	s_mov_b32 s8, s5
	s_mov_b32 s9, s5
	s_mov_b32 s10, s5
	s_mov_b32 s11, s5
	s_mov_b32 s12, s5
	s_waitcnt lgkmcnt(3)
	v_mfma_f32_32x32x16_f16 v[18:33], v[18:21], v[156:159], 0
	s_mov_b32 s13, s5
	s_mov_b32 s14, s5
	s_mov_b32 s15, s5
	s_mov_b32 s16, s5
	s_mov_b32 s17, s5
	s_mov_b32 s36, 1
	s_mov_b32 s34, -1
	s_waitcnt lgkmcnt(1)
	v_mfma_f32_32x32x16_f16 v[18:33], v[46:49], v[152:155], v[18:33]
	s_mov_b32 s35, 2
	s_mov_b64 s[30:31], 0x8000
	v_mfma_f32_32x32x16_f16 v[2:17], v[34:37], v[148:151], v[2:17]
	v_mfma_f32_32x32x16_f16 v[18:33], v[42:45], v[148:151], v[18:33]
	v_mfma_f32_32x32x16_f16 v[2:17], v[38:41], v[144:147], v[2:17]
	ds_read_b128 v[34:37], v172 offset:1024
	ds_read_b128 v[38:41], v172 offset:1536
	s_waitcnt lgkmcnt(2)
	v_mfma_f32_32x32x16_f16 v[18:33], v[50:53], v[144:147], v[18:33]
	s_waitcnt lgkmcnt(1)
	v_mfma_f32_32x32x16_f16 v[2:17], v[34:37], v[140:143], v[2:17]
	ds_read_b128 v[34:37], v172 offset:9216
	ds_read_b128 v[42:45], v172 offset:9728
	s_waitcnt lgkmcnt(1)
	v_mfma_f32_32x32x16_f16 v[18:33], v[34:37], v[140:143], v[18:33]
	ds_read_b128 v[34:37], v174 offset:1024
	ds_read_b128 v[46:49], v174 offset:1536
	s_waitcnt lgkmcnt(1)
	v_mfma_f32_32x32x16_f16 v[2:17], v[34:37], v[136:139], v[2:17]
	ds_read_b128 v[34:37], v174 offset:9216
	ds_read_b128 v[50:53], v174 offset:9728
	v_mfma_f32_32x32x16_f16 v[2:17], v[38:41], v[132:135], v[2:17]
	s_waitcnt lgkmcnt(1)
	v_mfma_f32_32x32x16_f16 v[18:33], v[34:37], v[136:139], v[18:33]
	v_mov_b32_e32 v34, 0xf149f2ca
	v_mfma_f32_32x32x16_f16 v[2:17], v[46:49], v[128:131], v[2:17]
	v_mfma_f32_32x32x16_f16 v[18:33], v[42:45], v[132:135], v[18:33]
	s_nop 10
	v_max_f32_e32 v35, v3, v3
	v_max_f32_e32 v36, v2, v2
	v_max_f32_e32 v35, v36, v35
	v_max3_f32 v35, v35, v4, v5
	v_max3_f32 v35, v35, v6, v7
	v_max3_f32 v35, v35, v8, v9
	v_max3_f32 v35, v35, v10, v11
	s_waitcnt lgkmcnt(0)
	v_mfma_f32_32x32x16_f16 v[18:33], v[50:53], v[128:131], v[18:33]
	v_max3_f32 v35, v35, v12, v13
	v_max3_f32 v35, v35, v14, v15
	v_max3_f32 v35, v35, v16, v17
	s_nop 8
	v_max3_f32 v35, v35, v18, v19
	v_max3_f32 v35, v35, v20, v21
	v_max3_f32 v35, v35, v22, v23
	v_max3_f32 v35, v35, v24, v25
	v_max3_f32 v35, v35, v26, v27
	v_max3_f32 v35, v35, v28, v29
	v_max3_f32 v35, v35, v30, v31
	v_max3_f32 v35, v35, v32, v33
	v_mov_b32_e32 v36, v35
	s_nop 1
	v_permlane32_swap_b32_e32 v35, v36
	v_max_f32_e32 v36, v36, v36
	v_max_f32_e32 v35, v35, v35
	v_max_f32_e32 v35, v35, v36
	v_add_f32_e32 v36, 0x7149f2ca, v35
	v_cmp_ge_f32_e32 vcc, s33, v36
	s_cmp_eq_u64 vcc, exec
	v_max_f32_e32 v35, 0xf149f2ca, v35
	s_cselect_b64 vcc, -1, 0
	v_cndmask_b32_e32 v168, v35, v34, vcc
	v_sub_f32_e32 v96, v18, v168
	v_sub_f32_e32 v97, v19, v168
	v_lshlrev_b32_e32 v18, 4, v0
	v_lshrrev_b32_e32 v19, 4, v0
	v_sub_f32_e32 v98, v20, v168
	v_and_b32_e32 v18, 0xc0, v18
	v_bitop3_b32 v19, v19, v54, 1 bitop3:0x6c
	v_lshlrev_b32_e32 v20, 3, v0
	v_sub_f32_e32 v99, v21, v168
	v_lshl_or_b32 v18, v54, 11, v18
	v_lshlrev_b32_e32 v19, 5, v19
	v_and_b32_e32 v21, 8, v20
	v_or3_b32 v18, v18, v21, v19
	v_and_b32_e32 v19, 16, v20
	v_sub_f32_e32 v0, 0xf149f2ca, v35
	v_add3_u32 v163, v19, s37, v18
	v_bitop3_b32 v169, v18, s4, v19 bitop3:0x36
	v_exp_f32_e32 v18, v0
	s_add_u32 s2, s2, s20
	v_sub_f32_e32 v2, v2, v168
	v_sub_f32_e32 v3, v3, v168
	v_sub_f32_e32 v4, v4, v168
	v_sub_f32_e32 v5, v5, v168
	v_sub_f32_e32 v6, v6, v168
	v_sub_f32_e32 v7, v7, v168
	v_sub_f32_e32 v8, v8, v168
	v_sub_f32_e32 v9, v9, v168
	v_sub_f32_e32 v10, v10, v168
	v_sub_f32_e32 v11, v11, v168
	v_sub_f32_e32 v12, v12, v168
	v_sub_f32_e32 v13, v13, v168
	v_sub_f32_e32 v14, v14, v168
	v_sub_f32_e32 v15, v15, v168
	v_sub_f32_e32 v16, v16, v168
	v_sub_f32_e32 v17, v17, v168
	s_addc_u32 s3, s3, s21
	s_mov_b32 s4, s5
	v_exp_f32_e32 v127, v2
	v_exp_f32_e32 v180, v3
	v_exp_f32_e32 v125, v4
	v_exp_f32_e32 v179, v5
	v_exp_f32_e32 v123, v6
	v_exp_f32_e32 v126, v7
	v_exp_f32_e32 v122, v8
	v_exp_f32_e32 v124, v9
	v_exp_f32_e32 v119, v10
	v_exp_f32_e32 v121, v11
	v_exp_f32_e32 v117, v12
	v_exp_f32_e32 v120, v13
	v_exp_f32_e32 v115, v14
	v_exp_f32_e32 v118, v15
	v_exp_f32_e32 v114, v16
	v_exp_f32_e32 v116, v17
	v_or3_b32 v0, s2, v1, v164
	v_mov_b32_e32 v1, s3
	v_lshlrev_b32_e32 v164, 3, v54
	v_mov_b64_e32 v[62:63], s[18:19]
	v_lshl_add_u64 v[0:1], s[22:23], 0, v[0:1]
	s_mov_b64 s[2:3], 0xc080
	v_mov_b64_e32 v[48:49], s[4:5]
	v_sub_f32_e32 v100, v22, v168
	v_sub_f32_e32 v101, v23, v168
	v_sub_f32_e32 v102, v24, v168
	v_sub_f32_e32 v103, v25, v168
	v_sub_f32_e32 v104, v26, v168
	v_sub_f32_e32 v105, v27, v168
	v_sub_f32_e32 v106, v28, v168
	v_sub_f32_e32 v107, v29, v168
	v_sub_f32_e32 v108, v30, v168
	v_sub_f32_e32 v109, v31, v168
	v_sub_f32_e32 v110, v32, v168
	v_sub_f32_e32 v111, v33, v168
	v_lshl_add_u64 v[170:171], v[0:1], 0, s[2:3]
	s_movk_i32 s2, 0xbf80
	s_movk_i32 s20, 0xc000
	s_movk_i32 s22, 0xff80
	v_mov_b32_e32 v166, 1.0
	v_mov_b64_e32 v[60:61], s[16:17]
	v_mov_b64_e32 v[58:59], s[14:15]
	v_mov_b64_e32 v[56:57], s[12:13]
	v_mov_b64_e32 v[54:55], s[10:11]
	v_mov_b64_e32 v[52:53], s[8:9]
	v_mov_b64_e32 v[50:51], s[6:7]
	v_mov_b64_e32 v[32:33], v[48:49]
	v_mov_b64_e32 v[16:17], v[48:49]
	v_mov_b64_e32 v[0:1], v[48:49]
	s_mov_b32 s3, -1
	s_mov_b32 s21, -1
	s_mov_b32 s23, -1
	v_add_u32_e32 v167, s37, v169
	v_mov_b64_e32 v[34:35], v[50:51]
	v_mov_b64_e32 v[36:37], v[52:53]
	v_mov_b64_e32 v[38:39], v[54:55]
	v_mov_b64_e32 v[40:41], v[56:57]
	v_mov_b64_e32 v[42:43], v[58:59]
	v_mov_b64_e32 v[44:45], v[60:61]
	v_mov_b64_e32 v[46:47], v[62:63]
	v_mov_b64_e32 v[18:19], v[50:51]
	v_mov_b64_e32 v[20:21], v[52:53]
	v_mov_b64_e32 v[22:23], v[54:55]
	v_mov_b64_e32 v[24:25], v[56:57]
	v_mov_b64_e32 v[26:27], v[58:59]
	v_mov_b64_e32 v[28:29], v[60:61]
	v_mov_b64_e32 v[30:31], v[62:63]
	v_mov_b64_e32 v[2:3], v[50:51]
	v_mov_b64_e32 v[4:5], v[52:53]
	v_mov_b64_e32 v[6:7], v[54:55]
	v_mov_b64_e32 v[8:9], v[56:57]
	v_mov_b64_e32 v[10:11], v[58:59]
	v_mov_b64_e32 v[12:13], v[60:61]
	v_mov_b64_e32 v[14:15], v[62:63]
